# baseline (speedup 1.0000x reference)
_Z11attn_kernelPKDF16_S0_S0_PDF16_:
	s_bfe_u32 s26, s2, 0x20003
	s_load_dwordx8 s[4:11], s[0:1], 0x0
	s_lshr_b32 s1, s2, 2
	s_lshr_b32 s20, s2, 6
	v_readfirstlane_b32 s19, v0
	s_mov_b32 s21, 0
	s_lshl_b32 s27, s26, 8
	s_and_b32 s0, s2, 7
	s_and_b32 s1, s1, 8
	s_lshr_b32 s34, s19, 6
	s_lshr_b32 s55, s19, 6
	s_lshl_b64 s[12:13], s[20:21], 11
	s_xor_b32 s16, s27, 0x700
	s_or_b32 s18, s1, s0
	s_or_b32 s0, s12, s16
	s_lshl_b32 s24, s34, 5
	s_add_u32 s0, s0, s24
	s_addc_u32 s1, s13, 0
	s_lshl_b64 s[14:15], s[0:1], 10
	s_lshl_b64 s[0:1], s[0:1], 11
	s_waitcnt lgkmcnt(0)
	s_add_u32 s0, s4, s0
	s_addc_u32 s1, s5, s1
	s_lshl_b32 s33, s18, 6
	s_lshl_b32 s2, s18, 7
	s_add_u32 s2, s0, s2
	s_addc_u32 s3, s1, 0
	s_lshl_b32 s0, s20, 4
	s_or_b32 s20, s18, s0
	s_and_b32 s17, s19, 0x3fffffc0
	s_lshl_b64 s[0:1], s[20:21], 18
	s_add_u32 s28, s6, s0
	s_addc_u32 s29, s7, s1
	s_lshl_b32 s18, s34, 10
	s_add_u32 s6, s28, s18
	s_addc_u32 s7, s29, 0
	s_add_u32 s30, s8, s0
	s_addc_u32 s31, s9, s1
	s_lshl_b32 s0, s19, 4
	v_and_b32_e32 v207, 63, v0
	s_and_b32 s0, s0, 0xfffff000
	v_mov_b32_e32 v3, 0
	v_lshlrev_b32_e32 v2, 4, v207
	s_add_u32 s0, s30, s0
	v_lshl_add_u64 v[212:213], s[6:7], 0, v[2:3]
	s_addc_u32 s1, s31, 0
	s_lshr_b32 s6, s19, 2
	v_bfe_u32 v1, v0, 2, 4
	v_and_or_b32 v2, s6, 48, v1
	v_lshlrev_b32_e32 v2, 6, v2
	v_lshlrev_b32_e32 v209, 3, v0
	s_cmp_lg_u32 0, -1
	v_lshl_add_u64 v[4:5], s[0:1], 0, v[2:3]
	v_and_b32_e32 v208, 24, v209
	s_cselect_b32 s0, 0, 0
	v_and_b32_e32 v222, 31, v0
	v_lshlrev_b32_e32 v2, 1, v208
	s_add_i32 s35, s18, s0
	s_mov_b32 s0, m0
	s_mov_b32 m0, s35
	s_nop 0
	global_load_lds_dwordx4 v[212:213], off
	s_mov_b32 m0, s0
	v_bfe_u32 v211, v0, 5, 1
	v_lshl_add_u64 v[194:195], v[4:5], 0, v[2:3]
	s_add_i32 s39, s35, 0x6000
	s_mov_b32 s0, m0
	s_mov_b32 m0, s39
	s_nop 0
	global_load_lds_dwordx4 v[194:195], off
	s_mov_b32 m0, s0
	v_lshlrev_b32_e32 v2, 10, v222
	s_mov_b64 s[0:1], 0x2000
	v_lshl_or_b32 v210, v211, 3, v2
	v_lshl_add_u64 v[214:215], v[212:213], 0, s[0:1]
	s_add_i32 s36, s35, 0x2000
	s_mov_b32 s6, m0
	s_mov_b32 m0, s36
	s_nop 0
	global_load_lds_dwordx4 v[214:215], off
	s_mov_b32 m0, s6
	v_lshlrev_b32_e32 v2, 1, v210
	global_load_dwordx4 v[158:161], v2, s[2:3] nt
	global_load_dwordx4 v[154:157], v2, s[2:3] offset:32 nt
	global_load_dwordx4 v[150:153], v2, s[2:3] offset:64 nt
	global_load_dwordx4 v[146:149], v2, s[2:3] offset:96 nt
	v_lshlrev_b32_e32 v4, 10, v211
	v_lshlrev_b32_e32 v5, 4, v222
	v_add3_u32 v224, 0, v4, v5
	v_mov_b32_e32 v4, v3
	v_mov_b32_e32 v5, v3
	v_mov_b32_e32 v6, v3
	v_mov_b32_e32 v7, v3
	v_mov_b32_e32 v8, v3
	v_mov_b32_e32 v9, v3
	v_mov_b32_e32 v10, v3
	v_mov_b32_e32 v11, v3
	v_mov_b32_e32 v12, v3
	v_mov_b32_e32 v13, v3
	v_mov_b32_e32 v14, v3
	v_mov_b32_e32 v15, v3
	v_mov_b32_e32 v16, v3
	v_mov_b32_e32 v17, v3
	v_mov_b32_e32 v18, v3
	v_mov_b32_e32 v19, v3
	s_mov_b64 s[2:3], 0x4000
	s_add_i32 s37, s35, 0x4000
	v_lshl_add_u64 v[216:217], v[212:213], 0, s[2:3]
	s_mov_b32 s6, m0
	s_mov_b32 m0, s37
	s_nop 0
	global_load_lds_dwordx4 v[216:217], off
	s_mov_b32 m0, s6
	s_waitcnt vmcnt(3) lgkmcnt(0)
	s_barrier
	ds_read_b128 v[36:39], v224
	ds_read_b128 v[40:43], v224 offset:512
	s_mov_b64 s[6:7], 0x6000
	s_mov_b32 s41, 3
	s_movk_i32 s46, 0x2000
	s_movk_i32 s25, 0x4000
	s_sub_i32 s43, 0xbf, s16
	s_mov_b32 s45, 0x41000000
	s_mov_b64 s[18:19], 0xa000
	v_lshlrev_b32_e32 v226, 4, v211
	v_mov_b32_e32 v233, v3
	v_lshlrev_b32_e32 v206, 3, v207
	s_waitcnt vmcnt(3) lgkmcnt(1)
	v_mfma_f32_32x32x16_f16 v[20:35], v[36:39], v[158:161], v[4:19]
	s_waitcnt lgkmcnt(0)
	v_mfma_f32_32x32x16_f16 v[4:19], v[40:43], v[158:161], v[4:19]
	ds_read_b128 v[36:39], v224 offset:2048
	ds_read_b128 v[40:43], v224 offset:2560
	s_waitcnt vmcnt(2) lgkmcnt(1)
	v_mfma_f32_32x32x16_f16 v[20:35], v[36:39], v[154:157], v[20:35]
	s_waitcnt lgkmcnt(0)
	v_mfma_f32_32x32x16_f16 v[4:19], v[40:43], v[154:157], v[4:19]
	ds_read_b128 v[36:39], v224 offset:4096
	ds_read_b128 v[40:43], v224 offset:4608
	s_waitcnt vmcnt(1) lgkmcnt(1)
	v_mfma_f32_32x32x16_f16 v[20:35], v[36:39], v[150:153], v[20:35]
	s_waitcnt lgkmcnt(0)
	v_mfma_f32_32x32x16_f16 v[4:19], v[40:43], v[150:153], v[4:19]
	ds_read_b128 v[36:39], v224 offset:6144
	ds_read_b128 v[40:43], v224 offset:6656
	s_waitcnt vmcnt(0) lgkmcnt(1)
	v_mfma_f32_32x32x16_f16 v[20:35], v[36:39], v[146:149], v[20:35]
	s_waitcnt lgkmcnt(0)
	v_mfma_f32_32x32x16_f16 v[4:19], v[40:43], v[146:149], v[4:19]
	s_nop 15
	s_nop 7
	s_nop 0
	v_max3_f32 v2, v20, v21, v4
	v_max3_f32 v36, v22, v23, v5
	s_nop 0
	v_max3_f32 v2, v2, v6, v7
	v_max3_f32 v36, v36, v26, v27
	s_nop 0
	v_max3_f32 v2, v2, v24, v25
	v_max3_f32 v36, v36, v10, v11
	s_nop 0
	v_max3_f32 v2, v2, v8, v9
	v_max3_f32 v36, v36, v30, v31
	s_nop 0
	v_max3_f32 v2, v2, v28, v29
	v_max3_f32 v36, v36, v14, v15
	s_nop 0
	v_max3_f32 v2, v2, v12, v13
	v_max3_f32 v36, v36, v34, v35
	s_nop 0
	v_max3_f32 v2, v2, v32, v33
	v_max3_f32 v36, v36, v18, v19
	s_nop 0
	v_max3_f32 v2, v2, v16, v17
	s_nop 0
	v_max_f32_e32 v2, v2, v36
	s_nop 0
	v_mov_b32_e32 v36, v2
	s_nop 1
	v_permlane32_swap_b32_e32 v2, v36
	v_max_f32_e32 v2, v2, v36
	s_nop 0
	v_sub_f32_e32 v50, v34, v2
	v_add_f32_e32 v231, v3, v2
	v_sub_f32_e32 v51, v35, v2
	v_sub_f32_e32 v52, v4, v2
	v_sub_f32_e32 v53, v5, v2
	v_lshl_add_u64 v[4:5], v[212:213], 0, s[6:7]
	v_xor_b32_e32 v34, 0x80000000, v231
	v_mov_b32_e32 v35, v34
	v_mov_b32_e32 v36, v34
	v_mov_b32_e32 v37, v34
	v_mov_b32_e32 v38, v34
	v_mov_b32_e32 v39, v34
	v_mov_b32_e32 v40, v34
	v_mov_b32_e32 v41, v34
	v_mov_b32_e32 v42, v34
	v_mov_b32_e32 v43, v34
	v_mov_b32_e32 v44, v34
	v_mov_b32_e32 v45, v34
	v_mov_b32_e32 v46, v34
	v_mov_b32_e32 v47, v34
	v_mov_b32_e32 v48, v34
	v_mov_b32_e32 v49, v34
	s_waitcnt vmcnt(0) lgkmcnt(0)
	s_barrier
	s_mov_b32 s8, m0
	s_mov_b32 m0, s35
	s_nop 0
	global_load_lds_dwordx4 v[4:5], off
	s_mov_b32 m0, s8
	s_add_i32 s8, s35, 0x8000
	v_lshl_add_u64 v[4:5], v[194:195], 0, s[0:1]
	s_mov_b32 s0, m0
	s_mov_b32 m0, s8
	s_nop 0
	global_load_lds_dwordx4 v[4:5], off
	s_mov_b32 m0, s0
	ds_read_b128 v[190:193], v224 offset:8192
	ds_read_b128 v[186:189], v224 offset:8704
	ds_read_b128 v[182:185], v224 offset:10240
	ds_read_b128 v[178:181], v224 offset:10752
	ds_read_b128 v[174:177], v224 offset:12288
	ds_read_b128 v[170:173], v224 offset:12800
	ds_read_b128 v[166:169], v224 offset:14336
	ds_read_b128 v[162:165], v224 offset:14848
	v_sub_f32_e32 v20, v20, v2
	v_sub_f32_e32 v21, v21, v2
	v_sub_f32_e32 v22, v22, v2
	v_sub_f32_e32 v23, v23, v2
	v_sub_f32_e32 v24, v24, v2
	v_sub_f32_e32 v25, v25, v2
	v_sub_f32_e32 v26, v26, v2
	v_sub_f32_e32 v27, v27, v2
	v_sub_f32_e32 v28, v28, v2
	v_sub_f32_e32 v29, v29, v2
	v_sub_f32_e32 v30, v30, v2
	v_sub_f32_e32 v31, v31, v2
	v_sub_f32_e32 v32, v32, v2
	v_sub_f32_e32 v33, v33, v2
	v_sub_f32_e32 v6, v6, v2
	v_sub_f32_e32 v7, v7, v2
	v_sub_f32_e32 v8, v8, v2
	v_sub_f32_e32 v9, v9, v2
	v_sub_f32_e32 v10, v10, v2
	v_sub_f32_e32 v11, v11, v2
	v_sub_f32_e32 v12, v12, v2
	v_sub_f32_e32 v13, v13, v2
	v_sub_f32_e32 v14, v14, v2
	v_sub_f32_e32 v15, v15, v2
	v_sub_f32_e32 v16, v16, v2
	v_sub_f32_e32 v17, v17, v2
	v_sub_f32_e32 v18, v18, v2
	v_sub_f32_e32 v19, v19, v2
	v_lshlrev_b32_e32 v2, 1, v0
	v_and_b32_e32 v228, 32, v2
	v_lshlrev_b32_e32 v2, 4, v0
	v_exp_f32_e32 v81, v51
	v_exp_f32_e32 v66, v20
	v_exp_f32_e32 v67, v21
	v_exp_f32_e32 v68, v22
	v_exp_f32_e32 v69, v23
	v_exp_f32_e32 v70, v24
	v_exp_f32_e32 v71, v25
	v_exp_f32_e32 v72, v26
	v_exp_f32_e32 v73, v27
	v_exp_f32_e32 v74, v28
	v_exp_f32_e32 v75, v29
	v_exp_f32_e32 v76, v30
	v_exp_f32_e32 v77, v31
	v_exp_f32_e32 v78, v32
	v_exp_f32_e32 v79, v33
	v_exp_f32_e32 v80, v50
	v_exp_f32_e32 v65, v19
	v_exp_f32_e32 v50, v52
	v_exp_f32_e32 v51, v53
	v_exp_f32_e32 v52, v6
	v_exp_f32_e32 v53, v7
	v_exp_f32_e32 v54, v8
	v_exp_f32_e32 v55, v9
	v_exp_f32_e32 v56, v10
	v_exp_f32_e32 v57, v11
	v_exp_f32_e32 v58, v12
	v_exp_f32_e32 v59, v13
	v_exp_f32_e32 v60, v14
	v_exp_f32_e32 v61, v15
	v_exp_f32_e32 v62, v16
	v_exp_f32_e32 v63, v17
	v_exp_f32_e32 v64, v18
	v_and_b32_e32 v2, 0xc0, v2
	s_add_i32 s0, s16, 0x100
	v_lshl_or_b32 v230, v211, 8, v2
	v_add_u32_e32 v2, 0, v228
	v_mov_b32_e32 v16, v3
	v_mov_b32_e32 v17, v3
	s_lshr_b32 s42, s0, 6
	s_lshl_b32 s0, s17, 2
	s_waitcnt vmcnt(2) lgkmcnt(0)
	s_barrier
	v_add3_u32 v225, v2, v208, v230
	v_mov_b32_e32 v2, v3
	v_mov_b32_e32 v4, v3
	v_mov_b32_e32 v5, v3
	v_mov_b32_e32 v6, v3
	v_mov_b32_e32 v7, v3
	v_mov_b32_e32 v8, v3
	v_mov_b32_e32 v9, v3
	v_mov_b32_e32 v10, v3
	v_mov_b32_e32 v11, v3
	v_mov_b32_e32 v12, v3
	v_mov_b32_e32 v13, v3
	v_mov_b32_e32 v14, v3
	v_mov_b32_e32 v15, v3
	s_add_i32 s38, s0, 0
	v_mov_b64_e32 v[32:33], v[16:17]
	v_cmp_gt_u32_e64 s[0:1], 32, v207
	s_mov_b64 s[8:9], 0
	s_mov_b64 s[16:17], 0x8000
	v_lshl_add_u32 v223, v222, 2, s38
	v_mov_b64_e32 v[30:31], v[14:15]
	v_mov_b64_e32 v[28:29], v[12:13]
	v_mov_b64_e32 v[26:27], v[10:11]
	v_mov_b64_e32 v[24:25], v[8:9]
	v_mov_b64_e32 v[22:23], v[6:7]
	v_mov_b64_e32 v[20:21], v[4:5]
	v_mov_b64_e32 v[18:19], v[2:3]

.Lmsk_8179:
	v_readfirstlane_b32 s54, v0
	v_lshlrev_b32_e32 v160, 1, v210
	s_or_b32 s50, s12, s27
	s_lshr_b32 s54, s54, 6
	s_lshl_b32 s54, s54, 5
	s_add_u32 s50, s50, s54
	s_addc_u32 s51, s13, 0
	s_lshl_b64 s[50:51], s[50:51], 11
	s_add_u32 s50, s4, s50
	s_addc_u32 s51, s5, s51
	s_lshl_b32 s54, s33, 1
	s_add_u32 s50, s50, s54
	s_addc_u32 s51, s51, 0
	global_load_dwordx4 v[156:159], v160, s[50:51] nt
	global_load_dwordx4 v[152:155], v160, s[50:51] offset:32 nt
	global_load_dwordx4 v[148:151], v160, s[50:51] offset:64 nt
	global_load_dwordx4 v[144:147], v160, s[50:51] offset:96 nt
	v_exp_f32_e32 v86, v86
	v_exp_f32_e32 v87, v87
	v_exp_f32_e32 v88, v88
	v_exp_f32_e32 v89, v89
	s_waitcnt lgkmcnt(10)
	s_cmp_lt_u32 s55, 4
	s_cbranch_scc1 .Lmsk_8188
	v_mfma_f32_32x32x16_f16 v[2:17], v[138:141], v[102:105], v[2:17]
